# final combine phases: nt hint on the expert-output row loads
# speedup vs baseline: 1.0049x; 1.0049x over previous
; __device__ __forceinline__ void p_final(const Args& a, const Frame& F, int half) {
;     ...
;         f32x4* xr = (f32x4*)(a.out + (size_t)t * D) + F.lane;
;         const u32x2* x1p = (const u32x2*)x1_row(a.out, a.ws, t) + F.lane;
;         const f32x4* g2 = (const f32x4*)(mod + (t >> 13) * 6144 + 5120) + F.lane;
;         int rk[4]; float wk[4];
; #pragma unroll
;         for (int k = 0; k < 4; ++k) { rk[k] = rkn[k]; wk[k] = wkn[k]; }
;         u32x2 ok[4][4], xw[4];
; #pragma unroll
;         for (int j = 0; j < 4; ++j) { xw[j] = x1p[64 * j];
; #pragma unroll
;             for (int k = 0; k < 4; ++k) ok[j][k] = *((const u32x2*)(OUTK + (size_t)rk[k] * D) + F.lane + 64 * j); }
;         { const int tn = t + NGW; if (tn < tend) {
; #pragma unroll
;             for (int k = 0; k < 4; ++k) { rkn[k] = tok_row[tn * 4 + k] - rowbase; wkn[k] = ent_w[tn * 4 + k]; } } }
.LBB0_1240:
	s_add_i32 s9, s4, 0xffff8800
	s_cmpk_lt_i32 s4, 0x7800
	s_cselect_b32 s27, s5, 0
	s_cselect_b32 s26, s4, s9
	s_waitcnt vmcnt(4)
	v_ashrrev_i32_e32 v23, 31, v4
	v_mov_b32_e32 v22, v4
	s_cselect_b32 s9, s22, s20
	s_cselect_b32 s28, s21, s19
	s_lshl_b64 s[26:27], s[26:27], 11
	v_lshlrev_b64 v[22:23], 11, v[22:23]
	s_add_u32 s26, s28, s26
	v_ashrrev_i32_e32 v19, 31, v2
	v_mov_b32_e32 v18, v2
	v_ashrrev_i32_e32 v21, 31, v3
	v_mov_b32_e32 v20, v3
	v_lshl_add_u64 v[70:71], v[14:15], 0, v[22:23]
	v_ashrrev_i32_e32 v23, 31, v5
	v_mov_b32_e32 v22, v5
	s_addc_u32 s27, s9, s27
	v_lshlrev_b64 v[18:19], 11, v[18:19]
	v_lshlrev_b64 v[20:21], 11, v[20:21]
	v_lshlrev_b64 v[22:23], 11, v[22:23]
	v_lshl_add_u64 v[18:19], v[14:15], 0, v[18:19]
	v_lshl_add_u64 v[20:21], v[14:15], 0, v[20:21]
	v_lshl_add_u64 v[72:73], v[14:15], 0, v[22:23]
	global_load_dwordx2 v[52:53], v67, s[26:27]
	global_load_dwordx2 v[42:43], v67, s[26:27] offset:512
	global_load_dwordx2 v[32:33], v67, s[26:27] offset:1024
	global_load_dwordx2 v[22:23], v67, s[26:27] offset:1536
	global_load_dwordx2 v[54:55], v[18:19], off nt
	global_load_dwordx2 v[44:45], v[18:19], off offset:512 nt
	global_load_dwordx2 v[34:35], v[18:19], off offset:1024 nt
	global_load_dwordx2 v[28:29], v[18:19], off offset:1536 nt
	global_load_dwordx2 v[56:57], v[20:21], off nt
	global_load_dwordx2 v[46:47], v[20:21], off offset:512 nt
	global_load_dwordx2 v[36:37], v[20:21], off offset:1024 nt
	global_load_dwordx2 v[30:31], v[20:21], off offset:1536 nt
	global_load_dwordx2 v[58:59], v[70:71], off nt
	global_load_dwordx2 v[48:49], v[70:71], off offset:512 nt
	global_load_dwordx2 v[38:39], v[70:71], off offset:1024 nt
	global_load_dwordx2 v[24:25], v[70:71], off offset:1536 nt
	global_load_dwordx2 v[60:61], v[72:73], off nt
	global_load_dwordx2 v[50:51], v[72:73], off offset:512 nt
	global_load_dwordx2 v[40:41], v[72:73], off offset:1024 nt
	global_load_dwordx2 v[26:27], v[72:73], off offset:1536 nt
	s_add_i32 s9, s6, s4
	s_cmp_ge_i32 s9, s14
	s_waitcnt vmcnt(24)
	v_mov_b64_e32 v[20:21], v[6:7]
	v_mov_b64_e32 v[18:19], v[8:9]
	s_cbranch_scc1 .LBB0_1239
	s_add_i32 s26, s8, -3
	s_ashr_i32 s27, s26, 31
	s_lshl_b64 s[26:27], s[26:27], 2
	s_add_u32 s28, s15, s26
	s_addc_u32 s29, s16, s27
	s_add_u32 s26, s17, s26
	s_addc_u32 s27, s18, s27
	s_add_i32 s34, s8, -2
	s_ashr_i32 s35, s34, 31
	s_lshl_b64 s[34:35], s[34:35], 2
	s_add_u32 s36, s15, s34
	s_addc_u32 s37, s16, s35
	s_add_u32 s34, s17, s34
	s_addc_u32 s35, s18, s35
	s_add_i32 s38, s8, -1
	s_ashr_i32 s39, s38, 31
	s_lshl_b64 s[38:39], s[38:39], 2
	s_add_u32 s40, s15, s38
	s_addc_u32 s41, s16, s39
	s_add_u32 s38, s17, s38
	s_addc_u32 s39, s18, s39
	s_ashr_i32 s9, s8, 31
	s_lshl_b64 s[42:43], s[8:9], 2
	s_add_u32 s44, s15, s42
	s_addc_u32 s45, s16, s43
	s_add_u32 s42, s17, s42
	s_addc_u32 s43, s18, s43
	global_load_dword v2, v11, s[28:29]
	global_load_dword v20, v11, s[26:27]
	global_load_dword v3, v11, s[36:37]
	global_load_dword v21, v11, s[34:35]
	global_load_dword v4, v11, s[40:41]
	global_load_dword v18, v11, s[38:39]
	global_load_dword v5, v11, s[44:45]
	global_load_dword v19, v11, s[42:43]
	s_branch .LBB0_1239

; __device__ __forceinline__ void p_final(const Args& a, const Frame& F, int half) {
;     ...
;         f32x4* xr = (f32x4*)(a.out + (size_t)t * D) + F.lane;
;         const u32x2* x1p = (const u32x2*)x1_row(a.out, a.ws, t) + F.lane;
;         const f32x4* g2 = (const f32x4*)(mod + (t >> 13) * 6144 + 5120) + F.lane;
;         int rk[4]; float wk[4];
; #pragma unroll
;         for (int k = 0; k < 4; ++k) { rk[k] = rkn[k]; wk[k] = wkn[k]; }
;         u32x2 ok[4][4], xw[4];
; #pragma unroll
;         for (int j = 0; j < 4; ++j) { xw[j] = x1p[64 * j];
; #pragma unroll
;             for (int k = 0; k < 4; ++k) ok[j][k] = *((const u32x2*)(OUTK + (size_t)rk[k] * D) + F.lane + 64 * j); }
;         { const int tn = t + NGW; if (tn < tend) {
; #pragma unroll
;             for (int k = 0; k < 4; ++k) { rkn[k] = tok_row[tn * 4 + k] - rowbase; wkn[k] = ent_w[tn * 4 + k]; } } }
.LBB0_1396:
	s_add_i32 s7, s0, 0xffff8800
	s_cmpk_lt_i32 s0, 0x7800
	s_cselect_b32 s23, s1, 0
	s_cselect_b32 s22, s0, s7
	v_ashrrev_i32_e32 v21, 31, v14
	v_mov_b32_e32 v20, v14
	s_cselect_b32 s7, s18, s16
	s_cselect_b32 s21, s17, s15
	s_lshl_b64 s[22:23], s[22:23], 11
	v_lshlrev_b64 v[20:21], 11, v[20:21]
	s_add_u32 s22, s21, s22
	v_ashrrev_i32_e32 v17, 31, v12
	v_mov_b32_e32 v16, v12
	v_ashrrev_i32_e32 v19, 31, v13
	v_mov_b32_e32 v18, v13
	v_lshl_add_u64 v[70:71], v[8:9], 0, v[20:21]
	v_ashrrev_i32_e32 v21, 31, v15
	v_mov_b32_e32 v20, v15
	s_addc_u32 s23, s7, s23
	v_lshlrev_b64 v[16:17], 11, v[16:17]
	v_lshlrev_b64 v[18:19], 11, v[18:19]
	v_lshlrev_b64 v[20:21], 11, v[20:21]
	v_lshl_add_u64 v[16:17], v[8:9], 0, v[16:17]
	v_lshl_add_u64 v[18:19], v[8:9], 0, v[18:19]
	v_lshl_add_u64 v[72:73], v[8:9], 0, v[20:21]
	global_load_dwordx2 v[50:51], v60, s[22:23]
	global_load_dwordx2 v[40:41], v60, s[22:23] offset:512
	global_load_dwordx2 v[30:31], v60, s[22:23] offset:1024
	global_load_dwordx2 v[20:21], v60, s[22:23] offset:1536
	global_load_dwordx2 v[52:53], v[16:17], off nt
	global_load_dwordx2 v[42:43], v[16:17], off offset:512 nt
	global_load_dwordx2 v[32:33], v[16:17], off offset:1024 nt
	global_load_dwordx2 v[26:27], v[16:17], off offset:1536 nt
	global_load_dwordx2 v[54:55], v[18:19], off nt
	global_load_dwordx2 v[44:45], v[18:19], off offset:512 nt
	global_load_dwordx2 v[34:35], v[18:19], off offset:1024 nt
	global_load_dwordx2 v[28:29], v[18:19], off offset:1536 nt
	global_load_dwordx2 v[56:57], v[70:71], off nt
	global_load_dwordx2 v[46:47], v[70:71], off offset:512 nt
	global_load_dwordx2 v[36:37], v[70:71], off offset:1024 nt
	global_load_dwordx2 v[22:23], v[70:71], off offset:1536 nt
	global_load_dwordx2 v[58:59], v[72:73], off nt
	global_load_dwordx2 v[48:49], v[72:73], off offset:512 nt
	global_load_dwordx2 v[38:39], v[72:73], off offset:1024 nt
	global_load_dwordx2 v[24:25], v[72:73], off offset:1536 nt
	s_add_i32 s7, s2, s0
	s_cmp_gt_i32 s7, 0xffff
	s_waitcnt vmcnt(24)
	v_mov_b64_e32 v[18:19], v[0:1]
	v_mov_b64_e32 v[16:17], v[2:3]
	s_cbranch_scc1 .LBB0_1395
	s_add_i32 s22, s6, -3
	s_ashr_i32 s23, s22, 31
	s_lshl_b64 s[22:23], s[22:23], 2
	s_add_u32 s24, s10, s22
	s_addc_u32 s25, s11, s23
	s_add_u32 s22, s12, s22
	s_addc_u32 s23, s13, s23
	s_add_i32 s26, s6, -2
	s_ashr_i32 s27, s26, 31
	s_lshl_b64 s[26:27], s[26:27], 2
	s_add_u32 s28, s10, s26
	s_addc_u32 s29, s11, s27
	s_add_u32 s26, s12, s26
	s_addc_u32 s27, s13, s27
	s_add_i32 s30, s6, -1
	s_ashr_i32 s31, s30, 31
	s_lshl_b64 s[30:31], s[30:31], 2
	s_add_u32 s34, s10, s30
	s_addc_u32 s35, s11, s31
	s_add_u32 s30, s12, s30
	s_addc_u32 s31, s13, s31
	s_ashr_i32 s7, s6, 31
	s_lshl_b64 s[36:37], s[6:7], 2
	s_add_u32 s38, s10, s36
	s_addc_u32 s39, s11, s37
	s_add_u32 s36, s12, s36
	s_addc_u32 s37, s13, s37
	global_load_dword v4, v5, s[24:25]
	global_load_dword v18, v5, s[22:23]
	global_load_dword v12, v5, s[28:29]
	global_load_dword v19, v5, s[26:27]
	global_load_dword v14, v5, s[34:35]
	global_load_dword v16, v5, s[30:31]
	global_load_dword v15, v5, s[38:39]
	global_load_dword v17, v5, s[36:37]
	s_waitcnt vmcnt(5)
	v_sub_u32_e32 v13, v12, v61
	v_sub_u32_e32 v12, v4, v61
	s_waitcnt vmcnt(3)
	v_sub_u32_e32 v14, v14, v61
	s_waitcnt vmcnt(1)
	v_sub_u32_e32 v15, v15, v61
	s_branch .LBB0_1395
